# v034-node-store-epilogue-deserialised
# baseline (speedup 1.0000x reference)
.LBB7_13:
	v_lshlrev_b32_e32 v96, 4, v147
	ds_read_b128 v[98:101], v96 offset:34816
	v_cvt_pk_f16_f32 v105, v88, v89
	v_cvt_pk_f16_f32 v104, v90, v91
	v_cvt_pk_f16_f32 v103, v92, v93
	v_cvt_pk_f16_f32 v102, v94, v95
	ds_read_b128 v[88:91], v96 offset:35840
	v_cvt_pk_f16_f32 v95, v48, v49
	v_cvt_pk_f16_f32 v94, v82, v83
	v_cvt_pk_f16_f32 v93, v84, v85
	s_waitcnt lgkmcnt(1)
	v_mfma_f32_32x32x16_f16 v[18:33], v[98:101], v[102:105], v[18:33]
	v_cvt_pk_f16_f32 v92, v86, v87
	ds_read_b128 v[82:85], v96 offset:36864
	v_cvt_pk_f16_f32 v87, v44, v45
	v_cvt_pk_f16_f32 v86, v46, v47
	v_cvt_pk_f16_f32 v47, v0, v1
	v_cvt_pk_f16_f32 v46, v34, v35
	v_cvt_pk_f16_f32 v45, v36, v37
	s_waitcnt lgkmcnt(1)
	v_mfma_f32_32x32x16_f16 v[18:33], v[88:91], v[92:95], v[18:33]
	v_cvt_pk_f16_f32 v89, v40, v41
	v_cvt_pk_f16_f32 v88, v42, v43
	ds_read_b128 v[40:43], v96 offset:37888
	v_cvt_pk_f16_f32 v44, v38, v39
	v_ashrrev_i32_e32 v107, 31, v106
	v_lshlrev_b64 v[0:1], 13, v[106:107]
	v_lshl_add_u64 v[0:1], s[2:3], 0, v[0:1]
	s_waitcnt lgkmcnt(1)
	v_mfma_f32_32x32x16_f16 v[18:33], v[82:85], v[86:89], v[18:33]
	v_add_u32_e32 v85, v148, v144
	v_lshl_add_u32 v84, v143, 2, v145
	s_waitcnt lgkmcnt(0)
	v_mfma_f32_32x32x16_f16 v[18:33], v[40:43], v[44:47], v[18:33]
	ds_read_b128 v[34:37], v96 offset:38912
	ds_read_b128 v[38:41], v96 offset:39936
	s_waitcnt lgkmcnt(1)
	v_mfma_f32_32x32x16_f16 v[2:17], v[34:37], v[102:105], v[2:17]
	s_waitcnt lgkmcnt(0)
	v_mfma_f32_32x32x16_f16 v[2:17], v[38:41], v[92:95], v[2:17]
	ds_read_b128 v[34:37], v96 offset:40960
	ds_read_b128 v[38:41], v96 offset:41984
	s_nop 3
	ds_write_b128 v85, v[18:21]
	ds_write_b128 v85, v[22:25] offset:32
	ds_write_b128 v85, v[26:29] offset:64
	ds_write_b128 v85, v[30:33] offset:96
	s_waitcnt lgkmcnt(5)
	v_mfma_f32_32x32x16_f16 v[2:17], v[34:37], v[86:89], v[2:17]
	v_min_i32_e32 v34, 32, v146
	v_lshlrev_b32_e32 v35, 2, v147
	v_cmp_lt_i32_e64 s[2:3], v142, v34
	v_lshlrev_b32_e32 v82, 2, v35
	s_waitcnt lgkmcnt(4)
	v_mfma_f32_32x32x16_f16 v[2:17], v[38:41], v[44:47], v[2:17]
	s_nop 11
	ds_write_b128 v85, v[2:5] offset:128
	ds_write_b128 v85, v[6:9] offset:160
	ds_write_b128 v85, v[10:13] offset:192
	ds_write_b128 v85, v[14:17] offset:224
	v_cmp_lt_i32_e64 s[2:3], v142, v34
	v_cmp_lt_i32_e64 s[4:5], v140, v34
	v_cmp_lt_i32_e64 s[6:7], v139, v34
	v_cmp_lt_i32_e64 s[8:9], v138, v34
	v_cmp_lt_i32_e64 s[10:11], v137, v34
	v_cmp_lt_i32_e64 s[12:13], v136, v34
	v_cmp_lt_i32_e64 s[14:15], v135, v34
	v_cmp_lt_i32_e64 s[16:17], v134, v34
	s_movk_i32 s22, 0x110
	v_add_u32_e32 v35, v84, v141
	ds_read_b128 v[156:159], v35
	v_mad_u32_u24 v36, v140, s22, v84
	ds_read_b128 v[160:163], v36
	v_mad_u32_u24 v35, v139, s22, v84
	ds_read_b128 v[164:167], v35
	v_mad_u32_u24 v36, v138, s22, v84
	ds_read_b128 v[168:171], v36
	v_mad_u32_u24 v35, v137, s22, v84
	ds_read_b128 v[172:175], v35
	v_mad_u32_u24 v36, v136, s22, v84
	ds_read_b128 v[176:179], v36
	v_mad_u32_u24 v35, v135, s22, v84
	ds_read_b128 v[180:183], v35
	v_mad_u32_u24 v36, v134, s22, v84
	ds_read_b128 v[184:187], v36
	v_mov_b32_e32 v83, 0
	v_lshl_add_u64 v[40:41], v[0:1], 0, v[82:83]
	s_mov_b64 s[22:23], 0x1000
	v_lshl_add_u64 v[188:189], v[40:41], 0, s[22:23]
	s_and_saveexec_b64 s[0:1], s[2:3]
	s_waitcnt lgkmcnt(7)
	global_store_dwordx4 v[40:41], v[156:159], off sc1
	s_or_b64 exec, exec, s[0:1]
	s_and_saveexec_b64 s[0:1], s[4:5]
	s_waitcnt lgkmcnt(6)
	global_store_dwordx4 v[40:41], v[160:163], off offset:1024 sc1
	s_or_b64 exec, exec, s[0:1]
	s_and_saveexec_b64 s[0:1], s[6:7]
	s_waitcnt lgkmcnt(5)
	global_store_dwordx4 v[40:41], v[164:167], off offset:2048 sc1
	s_or_b64 exec, exec, s[0:1]
	s_and_saveexec_b64 s[0:1], s[8:9]
	s_waitcnt lgkmcnt(4)
	global_store_dwordx4 v[40:41], v[168:171], off offset:3072 sc1
	s_or_b64 exec, exec, s[0:1]
	s_and_saveexec_b64 s[0:1], s[10:11]
	s_waitcnt lgkmcnt(3)
	global_store_dwordx4 v[188:189], v[172:175], off sc1
	s_or_b64 exec, exec, s[0:1]
	s_and_saveexec_b64 s[0:1], s[12:13]
	s_waitcnt lgkmcnt(2)
	global_store_dwordx4 v[188:189], v[176:179], off offset:1024 sc1
	s_or_b64 exec, exec, s[0:1]
	s_and_saveexec_b64 s[0:1], s[14:15]
	s_waitcnt lgkmcnt(1)
	global_store_dwordx4 v[188:189], v[180:183], off offset:2048 sc1
	s_or_b64 exec, exec, s[0:1]
	s_and_saveexec_b64 s[0:1], s[16:17]
	s_waitcnt lgkmcnt(0)
	global_store_dwordx4 v[188:189], v[184:187], off offset:3072 sc1
	s_or_b64 exec, exec, s[0:1]

.LBB7_31:
	v_or_b32_e32 v83, 0x8800, v96
	ds_read_b128 v[34:37], v83 offset:16384
	v_cvt_pk_f16_f32 v25, v24, v25
	v_cvt_pk_f16_f32 v24, v22, v23
	v_cvt_pk_f16_f32 v23, v20, v21
	v_cvt_pk_f16_f32 v22, v18, v19
	ds_read_b128 v[18:21], v83 offset:17408
	v_cvt_pk_f16_f32 v33, v32, v33
	v_cvt_pk_f16_f32 v32, v30, v31
	v_cvt_pk_f16_f32 v31, v28, v29
	s_waitcnt lgkmcnt(1)
	v_mfma_f32_32x32x16_f16 v[34:49], v[34:37], v[22:25], 0
	v_cvt_pk_f16_f32 v30, v26, v27
	v_cvt_pk_f16_f32 v29, v8, v9
	v_cvt_pk_f16_f32 v28, v6, v7
	v_cvt_pk_f16_f32 v27, v4, v5
	v_cvt_pk_f16_f32 v26, v2, v3
	v_lshlrev_b64 v[90:91], 11, v[106:107]
	ds_read_b128 v[0:3], v83 offset:19456
	s_waitcnt lgkmcnt(1)
	v_mfma_f32_32x32x16_f16 v[34:49], v[18:21], v[30:33], v[34:49]
	ds_read_b128 v[18:21], v83 offset:18432
	ds_read_b128 v[4:7], v83 offset:20480
	ds_read_b128 v[86:89], v83 offset:21504
	s_waitcnt lgkmcnt(2)
	v_mfma_f32_32x32x16_f16 v[34:49], v[18:21], v[26:29], v[34:49]
	v_cvt_pk_f16_f32 v19, v16, v17
	v_cvt_pk_f16_f32 v18, v14, v15
	v_cvt_pk_f16_f32 v17, v12, v13
	v_cvt_pk_f16_f32 v16, v10, v11
	s_nop 1
	v_mfma_f32_32x32x16_f16 v[34:49], v[0:3], v[16:19], v[34:49]
	s_nop 11
	v_mul_f32_e32 v0, v34, v74
	v_mul_f32_e32 v1, v35, v75
	v_mul_f32_e32 v2, v36, v76
	v_mul_f32_e32 v3, v37, v77
	v_mul_f32_e32 v8, v38, v78
	v_mul_f32_e32 v9, v39, v79
	v_mul_f32_e32 v10, v40, v80
	v_mul_f32_e32 v11, v41, v81
	v_cvt_pk_f16_f32 v3, v37, v3
	v_cvt_pk_f16_f32 v2, v36, v2
	v_cvt_pk_f16_f32 v1, v35, v1
	v_cvt_pk_f16_f32 v0, v34, v0
	v_cvt_pk_f16_f32 v37, v41, v11
	v_cvt_pk_f16_f32 v36, v40, v10
	v_cvt_pk_f16_f32 v35, v39, v9
	v_cvt_pk_f16_f32 v34, v38, v8
	ds_write_b128 v85, v[0:3]
	s_waitcnt lgkmcnt(2)
	v_mfma_f32_32x32x16_f16 v[0:15], v[4:7], v[22:25], 0
	ds_write_b128 v85, v[34:37] offset:32
	ds_read_b128 v[34:37], v83 offset:22528
	v_mul_f32_e32 v20, v42, v70
	v_mul_f32_e32 v21, v43, v71
	v_mul_f32_e32 v22, v44, v72
	v_mul_f32_e32 v23, v45, v73
	v_cvt_pk_f16_f32 v23, v45, v23
	s_waitcnt lgkmcnt(3)
	v_mfma_f32_32x32x16_f16 v[0:15], v[86:89], v[30:33], v[0:15]
	v_cvt_pk_f16_f32 v22, v44, v22
	v_cvt_pk_f16_f32 v21, v43, v21
	v_cvt_pk_f16_f32 v20, v42, v20
	ds_write_b128 v85, v[20:23] offset:64
	ds_read_b128 v[20:23], v83 offset:23552
	v_mul_f32_e32 v24, v46, v66
	v_mul_f32_e32 v25, v47, v67
	s_waitcnt lgkmcnt(2)
	v_mfma_f32_32x32x16_f16 v[0:15], v[34:37], v[26:29], v[0:15]
	v_mul_f32_e32 v26, v48, v68
	v_mul_f32_e32 v27, v49, v69
	v_cvt_pk_f16_f32 v27, v49, v27
	v_cvt_pk_f16_f32 v26, v48, v26
	v_cvt_pk_f16_f32 v25, v47, v25
	v_cvt_pk_f16_f32 v24, v46, v24
	ds_write_b128 v85, v[24:27] offset:96
	s_waitcnt lgkmcnt(1)
	v_mfma_f32_32x32x16_f16 v[0:15], v[20:23], v[16:19], v[0:15]
	s_nop 11
	v_mul_f32_e32 v16, v0, v62
	v_mul_f32_e32 v17, v1, v63
	v_mul_f32_e32 v18, v2, v64
	v_mul_f32_e32 v19, v3, v65
	v_cvt_pk_f16_f32 v3, v3, v19
	v_cvt_pk_f16_f32 v2, v2, v18
	v_cvt_pk_f16_f32 v1, v1, v17
	v_cvt_pk_f16_f32 v0, v0, v16
	ds_write_b128 v85, v[0:3] offset:128
	v_mul_f32_e32 v0, v4, v58
	v_mul_f32_e32 v1, v5, v59
	v_mul_f32_e32 v2, v6, v60
	v_mul_f32_e32 v3, v7, v61
	v_cvt_pk_f16_f32 v3, v7, v3
	v_cvt_pk_f16_f32 v2, v6, v2
	v_cvt_pk_f16_f32 v1, v5, v1
	v_cvt_pk_f16_f32 v0, v4, v0
	ds_write_b128 v85, v[0:3] offset:160
	v_mul_f32_e32 v0, v8, v54
	v_mul_f32_e32 v1, v9, v55
	v_mul_f32_e32 v2, v10, v56
	v_mul_f32_e32 v3, v11, v57
	v_cvt_pk_f16_f32 v3, v11, v3
	v_cvt_pk_f16_f32 v2, v10, v2
	v_cvt_pk_f16_f32 v1, v9, v1
	v_cvt_pk_f16_f32 v0, v8, v0
	ds_write_b128 v85, v[0:3] offset:192
	v_mul_f32_e32 v0, v12, v50
	v_mul_f32_e32 v1, v13, v51
	v_mul_f32_e32 v2, v14, v52
	v_mul_f32_e32 v3, v15, v53
	v_cvt_pk_f16_f32 v3, v15, v3
	v_cvt_pk_f16_f32 v2, v14, v2
	v_cvt_pk_f16_f32 v1, v13, v1
	v_cvt_pk_f16_f32 v0, v12, v0
	ds_write_b128 v85, v[0:3] offset:224
	v_lshl_add_u64 v[0:1], v[90:91], 2, s[20:21]
	s_movk_i32 s22, 0x110
	v_add_u32_e32 v2, v84, v141
	ds_read_b128 v[156:159], v2
	v_mad_u32_u24 v3, v140, s22, v84
	ds_read_b128 v[160:163], v3
	v_mad_u32_u24 v2, v139, s22, v84
	ds_read_b128 v[164:167], v2
	v_mad_u32_u24 v3, v138, s22, v84
	ds_read_b128 v[168:171], v3
	v_mad_u32_u24 v2, v137, s22, v84
	ds_read_b128 v[172:175], v2
	v_mad_u32_u24 v3, v136, s22, v84
	ds_read_b128 v[176:179], v3
	v_mad_u32_u24 v2, v135, s22, v84
	ds_read_b128 v[180:183], v2
	v_mad_u32_u24 v3, v134, s22, v84
	ds_read_b128 v[184:187], v3
	v_mov_b32_e32 v83, 0
	v_lshl_add_u64 v[6:7], v[0:1], 0, v[82:83]
	s_mov_b64 s[22:23], 0x1000
	v_lshl_add_u64 v[188:189], v[6:7], 0, s[22:23]
	s_and_saveexec_b64 s[0:1], s[2:3]
	s_waitcnt lgkmcnt(7)
	global_store_dwordx4 v[6:7], v[156:159], off sc1
	s_or_b64 exec, exec, s[0:1]
	s_and_saveexec_b64 s[0:1], s[4:5]
	s_waitcnt lgkmcnt(6)
	global_store_dwordx4 v[6:7], v[160:163], off offset:1024 sc1
	s_or_b64 exec, exec, s[0:1]
	s_and_saveexec_b64 s[0:1], s[6:7]
	s_waitcnt lgkmcnt(5)
	global_store_dwordx4 v[6:7], v[164:167], off offset:2048 sc1
	s_or_b64 exec, exec, s[0:1]
	s_and_saveexec_b64 s[0:1], s[8:9]
	s_waitcnt lgkmcnt(4)
	global_store_dwordx4 v[6:7], v[168:171], off offset:3072 sc1
	s_or_b64 exec, exec, s[0:1]
	s_and_saveexec_b64 s[0:1], s[10:11]
	s_waitcnt lgkmcnt(3)
	global_store_dwordx4 v[188:189], v[172:175], off sc1
	s_or_b64 exec, exec, s[0:1]
	s_and_saveexec_b64 s[0:1], s[12:13]
	s_waitcnt lgkmcnt(2)
	global_store_dwordx4 v[188:189], v[176:179], off offset:1024 sc1
	s_or_b64 exec, exec, s[0:1]
	s_and_saveexec_b64 s[0:1], s[14:15]
	s_waitcnt lgkmcnt(1)
	global_store_dwordx4 v[188:189], v[180:183], off offset:2048 sc1
	s_or_b64 exec, exec, s[0:1]
	s_and_saveexec_b64 s[0:1], s[16:17]
	s_waitcnt lgkmcnt(0)
	global_store_dwordx4 v[188:189], v[184:187], off offset:3072 sc1
	s_or_b64 exec, exec, s[0:1]
	s_endpgm

	.amdhsa_kernel _Z6k_nodeILi0ELi0EEvPfS0_PDv2_DF16_PKiPKfS4_S0_S0_S4_S6_PKDv8_DF16_S6_S9_S6_S9_
		.amdhsa_group_segment_fixed_size 59392
		.amdhsa_private_segment_fixed_size 0
		.amdhsa_kernarg_size 120
		.amdhsa_user_sgpr_count 2
		.amdhsa_user_sgpr_dispatch_ptr 0
		.amdhsa_user_sgpr_queue_ptr 0
		.amdhsa_user_sgpr_kernarg_segment_ptr 1
		.amdhsa_user_sgpr_dispatch_id 0
		.amdhsa_user_sgpr_kernarg_preload_length 0
		.amdhsa_user_sgpr_kernarg_preload_offset 0
		.amdhsa_user_sgpr_private_segment_size 0
		.amdhsa_uses_dynamic_stack 0
		.amdhsa_enable_private_segment 0
		.amdhsa_system_sgpr_workgroup_id_x 1
		.amdhsa_system_sgpr_workgroup_id_y 0
		.amdhsa_system_sgpr_workgroup_id_z 0
		.amdhsa_system_sgpr_workgroup_info 0
		.amdhsa_system_vgpr_workitem_id 0
		.amdhsa_next_free_vgpr 190
		.amdhsa_next_free_sgpr 96
		.amdhsa_accum_offset 192
		.amdhsa_reserve_vcc 1
		.amdhsa_float_round_mode_32 0
		.amdhsa_float_round_mode_16_64 0
		.amdhsa_float_denorm_mode_32 3
		.amdhsa_float_denorm_mode_16_64 3
		.amdhsa_dx10_clamp 1
		.amdhsa_ieee_mode 1
		.amdhsa_fp16_overflow 0
		.amdhsa_tg_split 0
		.amdhsa_exception_fp_ieee_invalid_op 0
		.amdhsa_exception_fp_denorm_src 0
		.amdhsa_exception_fp_ieee_div_zero 0
		.amdhsa_exception_fp_ieee_overflow 0
		.amdhsa_exception_fp_ieee_underflow 0
		.amdhsa_exception_fp_ieee_inexact 0
		.amdhsa_exception_int_div_zero 0
	.end_amdhsa_kernel

.LBB8_13:
	v_lshlrev_b32_e32 v160, 4, v210
	ds_read_b128 v[162:165], v160 offset:34816
	v_cvt_pk_f16_f32 v169, v152, v153
	v_cvt_pk_f16_f32 v168, v154, v155
	v_cvt_pk_f16_f32 v167, v156, v157
	v_cvt_pk_f16_f32 v166, v158, v159
	ds_read_b128 v[152:155], v160 offset:35840
	v_cvt_pk_f16_f32 v159, v144, v145
	v_cvt_pk_f16_f32 v158, v146, v147
	v_cvt_pk_f16_f32 v157, v148, v149
	s_waitcnt lgkmcnt(1)
	v_mfma_f32_32x32x16_f16 v[18:33], v[162:165], v[166:169], v[18:33]
	v_cvt_pk_f16_f32 v156, v150, v151
	ds_read_b128 v[144:147], v160 offset:36864
	v_cvt_pk_f16_f32 v151, v136, v137
	v_cvt_pk_f16_f32 v150, v138, v139
	v_cvt_pk_f16_f32 v149, v140, v141
	v_cvt_pk_f16_f32 v148, v142, v143
	v_cvt_pk_f16_f32 v137, v134, v135
	s_waitcnt lgkmcnt(1)
	v_mfma_f32_32x32x16_f16 v[18:33], v[152:155], v[156:159], v[18:33]
	ds_read_b128 v[138:141], v160 offset:37888
	ds_read_b128 v[152:155], v160 offset:38912
	v_cvt_pk_f16_f32 v136, v0, v1
	v_cvt_pk_f16_f32 v135, v46, v47
	v_cvt_pk_f16_f32 v134, v132, v133
	s_mov_b32 s1, 0xbfb8aa3b
	s_mov_b32 s0, 0x3f317218
	s_waitcnt lgkmcnt(2)
	v_mfma_f32_32x32x16_f16 v[18:33], v[144:147], v[148:151], v[18:33]
	ds_read_b128 v[142:145], v160 offset:39936
	ds_read_b128 v[162:165], v160 offset:40960
	ds_read_b128 v[174:177], v160 offset:41984
	ds_write_b128 v212, v[104:107]
	ds_write_b128 v212, v[100:103] offset:1088
	ds_write_b128 v212, v[108:111] offset:2176
	ds_write_b128 v212, v[112:115] offset:3264
	ds_write_b128 v212, v[116:119] offset:4352
	ds_write_b128 v212, v[120:123] offset:5440
	ds_write_b128 v212, v[128:131] offset:6528
	v_add_u32_e32 v108, v211, v173
	ds_write_b128 v212, v[124:127] offset:7616
	v_ashrrev_i32_e32 v173, 31, v172
	s_waitcnt lgkmcnt(12)
	v_mfma_f32_32x32x16_f16 v[18:33], v[138:141], v[134:137], v[18:33]
	s_waitcnt lgkmcnt(11)
	v_mfma_f32_32x32x16_f16 v[2:17], v[152:155], v[166:169], v[2:17]
	s_nop 9
	v_mul_f32_e64 v0, |v18|, s1
	v_max_f32_e32 v1, v18, v18
	v_mul_f32_e64 v18, |v19|, s1
	v_exp_f32_e32 v18, v18
	v_exp_f32_e32 v0, v0
	v_max_f32_e32 v100, 0, v1
	v_add_f32_e32 v1, 1.0, v18
	v_max_f32_e32 v18, v19, v19
	v_mul_f32_e64 v19, |v21|, s1
	v_exp_f32_e32 v46, v19
	v_add_f32_e32 v0, 1.0, v0
	v_log_f32_e32 v101, v0
	v_log_f32_e32 v0, v1
	v_mul_f32_e64 v1, |v20|, s1
	v_max_f32_e32 v19, v20, v20
	v_add_f32_e32 v20, 1.0, v46
	v_mul_f32_e64 v46, |v22|, s1
	v_exp_f32_e32 v47, v46
	v_max_f32_e32 v21, v21, v21
	v_max_f32_e32 v46, 0, v21
	v_exp_f32_e32 v1, v1
	v_add_f32_e32 v21, 1.0, v47
	v_mul_f32_e64 v47, |v23|, s1
	v_exp_f32_e32 v102, v47
	v_max_f32_e32 v22, v22, v22
	v_max_f32_e32 v47, 0, v22
	v_add_f32_e32 v1, 1.0, v1
	v_add_f32_e32 v22, 1.0, v102
	v_mul_f32_e64 v102, |v24|, s1
	v_exp_f32_e32 v103, v102
	v_log_f32_e32 v1, v1
	v_max_f32_e32 v23, v23, v23
	v_log_f32_e32 v20, v20
	v_log_f32_e32 v21, v21
	v_max_f32_e32 v102, 0, v23
	v_add_f32_e32 v23, 1.0, v103
	v_log_f32_e32 v22, v22
	v_log_f32_e32 v23, v23
	v_max_f32_e32 v18, 0, v18
	v_max_f32_e32 v19, 0, v19
	v_mul_f32_e64 v103, |v25|, s1
	v_max_f32_e32 v24, v24, v24
	v_pk_fma_f32 v[0:1], v[0:1], s[0:1], v[18:19] op_sel_hi:[1,0,1]
	v_exp_f32_e32 v104, v103
	v_max_f32_e32 v103, 0, v24
	v_cvt_pk_f16_f32 v18, v0, v1
	v_pk_fma_f32 v[0:1], v[20:21], s[0:1], v[46:47] op_sel_hi:[1,0,1]
	s_waitcnt lgkmcnt(10)
	v_mfma_f32_32x32x16_f16 v[2:17], v[142:145], v[156:159], v[2:17]
	v_cvt_pk_f16_f32 v19, v0, v1
	v_fma_f32 v0, v22, s0, v102
	v_fma_f32 v1, v23, s0, v103
	v_add_f32_e32 v24, 1.0, v104
	v_cvt_pk_f16_f32 v0, v0, v1
	v_mul_f32_e64 v1, |v26|, s1
	v_exp_f32_e32 v1, v1
	v_alignbit_b32 v102, v0, v19, 16
	v_lshrrev_b32_e32 v103, 16, v0
	s_waitcnt lgkmcnt(9)
	v_mfma_f32_32x32x16_f16 v[2:17], v[162:165], v[148:151], v[2:17]
	v_add_f32_e32 v0, 1.0, v1
	v_mul_f32_e64 v1, |v27|, s1
	v_exp_f32_e32 v1, v1
	v_log_f32_e32 v24, v24
	v_log_f32_e32 v46, v0
	v_max_f32_e32 v0, v26, v26
	v_max_f32_e32 v25, v25, v25
	v_max_f32_e32 v47, 0, v0
	v_add_f32_e32 v0, 1.0, v1
	v_mul_f32_e64 v1, |v28|, s1
	v_max_f32_e32 v25, 0, v25
	v_fma_mixlo_f16 v100, v101, s0, v100
	v_alignbit_b32 v101, v19, v18, 16
	v_exp_f32_e32 v1, v1
	v_mul_f32_e64 v19, |v29|, s1
	v_mul_f32_e64 v21, |v30|, s1
	v_fma_mixhi_f16 v103, v24, s0, v25
	v_exp_f32_e32 v20, v19
	v_exp_f32_e32 v21, v21
	v_mul_f32_e64 v23, |v31|, s1
	v_mul_f32_e64 v25, |v32|, s1
	v_exp_f32_e32 v24, v23
	v_exp_f32_e32 v25, v25
	s_waitcnt lgkmcnt(8)
	v_mfma_f32_32x32x16_f16 v[2:17], v[174:177], v[134:137], v[2:17]
	v_add_f32_e32 v1, 1.0, v1
	v_log_f32_e32 v0, v0
	v_log_f32_e32 v1, v1
	v_add_f32_e32 v20, 1.0, v20
	v_add_f32_e32 v21, 1.0, v21
	v_log_f32_e32 v20, v20
	v_log_f32_e32 v21, v21
	v_add_f32_e32 v24, 1.0, v24
	v_add_f32_e32 v25, 1.0, v25
	v_pack_b32_f16 v100, v100, v18
	v_max_f32_e32 v18, v27, v27
	v_max_f32_e32 v19, v28, v28
	v_log_f32_e32 v24, v24
	v_log_f32_e32 v25, v25
	v_max_f32_e32 v18, 0, v18
	v_max_f32_e32 v19, 0, v19
	v_max_f32_e32 v22, v29, v29
	v_max_f32_e32 v23, v30, v30
	v_mul_f32_e64 v27, |v33|, s1
	v_max_f32_e32 v22, 0, v22
	v_max_f32_e32 v23, 0, v23
	v_max_f32_e32 v26, v31, v31
	v_exp_f32_e32 v28, v27
	v_max_f32_e32 v27, v32, v32
	v_pk_fma_f32 v[0:1], v[0:1], s[0:1], v[18:19] op_sel_hi:[1,0,1]
	v_max_f32_e32 v26, 0, v26
	v_max_f32_e32 v27, 0, v27
	v_cvt_pk_f16_f32 v18, v0, v1
	v_pk_fma_f32 v[0:1], v[20:21], s[0:1], v[22:23] op_sel_hi:[1,0,1]
	v_fma_mixlo_f16 v30, v46, s0, v47
	v_cvt_pk_f16_f32 v19, v0, v1
	v_pk_fma_f32 v[0:1], v[24:25], s[0:1], v[26:27] op_sel_hi:[1,0,1]
	v_pack_b32_f16 v104, v30, v18
	v_cvt_pk_f16_f32 v0, v0, v1
	v_mul_f32_e64 v1, |v2|, s1
	v_exp_f32_e32 v1, v1
	v_alignbit_b32 v106, v0, v19, 16
	v_lshrrev_b32_e32 v107, 16, v0
	v_alignbit_b32 v105, v19, v18, 16
	v_add_f32_e32 v0, 1.0, v1
	v_mul_f32_e64 v1, |v3|, s1
	v_log_f32_e32 v22, v0
	v_max_f32_e32 v0, v2, v2
	v_max_f32_e32 v2, v3, v3
	v_mul_f32_e64 v3, |v5|, s1
	v_exp_f32_e32 v1, v1
	v_exp_f32_e32 v18, v3
	v_max_f32_e32 v23, 0, v0
	v_max_f32_e32 v3, v4, v4
	v_add_f32_e32 v0, 1.0, v1
	v_mul_f32_e64 v1, |v4|, s1
	v_add_f32_e32 v4, 1.0, v18
	v_mul_f32_e64 v18, |v6|, s1
	v_exp_f32_e32 v19, v18
	v_max_f32_e32 v5, v5, v5
	v_max_f32_e32 v18, 0, v5
	v_exp_f32_e32 v1, v1
	v_add_f32_e32 v5, 1.0, v19
	v_mul_f32_e64 v19, |v7|, s1
	v_exp_f32_e32 v20, v19
	v_max_f32_e32 v6, v6, v6
	v_max_f32_e32 v19, 0, v6
	v_add_f32_e32 v1, 1.0, v1
	v_add_f32_e32 v6, 1.0, v20
	v_mul_f32_e64 v20, |v8|, s1
	v_exp_f32_e32 v21, v20
	v_log_f32_e32 v0, v0
	v_log_f32_e32 v1, v1
	v_max_f32_e32 v7, v7, v7
	v_log_f32_e32 v4, v4
	v_log_f32_e32 v5, v5
	v_max_f32_e32 v20, 0, v7
	v_add_f32_e32 v7, 1.0, v21
	v_log_f32_e32 v6, v6
	v_log_f32_e32 v7, v7
	v_max_f32_e32 v2, 0, v2
	v_max_f32_e32 v3, 0, v3
	v_mul_f32_e64 v21, |v9|, s1
	v_max_f32_e32 v8, v8, v8
	v_pk_fma_f32 v[0:1], v[0:1], s[0:1], v[2:3] op_sel_hi:[1,0,1]
	v_exp_f32_e32 v24, v21
	v_max_f32_e32 v21, 0, v8
	v_cvt_pk_f16_f32 v2, v0, v1
	v_pk_fma_f32 v[0:1], v[4:5], s[0:1], v[18:19] op_sel_hi:[1,0,1]
	v_add_f32_e32 v28, 1.0, v28
	v_cvt_pk_f16_f32 v3, v0, v1
	v_pk_fma_f32 v[0:1], v[6:7], s[0:1], v[20:21] op_sel_hi:[1,0,1]
	v_log_f32_e32 v28, v28
	v_cvt_pk_f16_f32 v0, v0, v1
	v_mul_f32_e64 v1, |v10|, s1
	v_exp_f32_e32 v1, v1
	v_alignbit_b32 v112, v0, v3, 16
	v_lshrrev_b32_e32 v113, 16, v0
	v_max_f32_e32 v29, v33, v33
	v_add_f32_e32 v0, 1.0, v1
	v_mul_f32_e64 v1, |v11|, s1
	v_exp_f32_e32 v1, v1
	v_log_f32_e32 v109, v0
	v_max_f32_e32 v0, v10, v10
	v_max_f32_e32 v116, 0, v0
	v_add_f32_e32 v0, 1.0, v1
	v_mul_f32_e64 v1, |v12|, s1
	v_exp_f32_e32 v1, v1
	v_max_f32_e32 v29, 0, v29
	v_log_f32_e32 v26, v0
	v_max_f32_e32 v0, v11, v11
	v_fma_mixhi_f16 v107, v28, s0, v29
	v_max_f32_e32 v28, 0, v0
	v_add_f32_e32 v0, 1.0, v1
	v_mul_f32_e64 v1, |v13|, s1
	v_exp_f32_e32 v1, v1
	v_log_f32_e32 v27, v0
	v_max_f32_e32 v0, v12, v12
	v_max_f32_e32 v29, 0, v0
	v_add_f32_e32 v0, 1.0, v1
	v_mul_f32_e64 v1, |v14|, s1
	v_exp_f32_e32 v1, v1
	v_log_f32_e32 v30, v0
	v_max_f32_e32 v0, v13, v13
	v_max_f32_e32 v32, 0, v0
	v_add_f32_e32 v0, 1.0, v1
	v_mul_f32_e64 v1, |v15|, s1
	v_exp_f32_e32 v1, v1
	v_log_f32_e32 v31, v0
	v_max_f32_e32 v0, v14, v14
	v_max_f32_e32 v33, 0, v0
	v_add_f32_e32 v0, 1.0, v1
	v_mul_f32_e64 v1, |v16|, s1
	v_add_f32_e32 v8, 1.0, v24
	v_exp_f32_e32 v1, v1
	v_log_f32_e32 v8, v8
	v_max_f32_e32 v9, v9, v9
	v_log_f32_e32 v46, v0
	v_max_f32_e32 v0, v15, v15
	v_max_f32_e32 v9, 0, v9
	v_fma_mixlo_f16 v22, v22, s0, v23
	v_max_f32_e32 v114, 0, v0
	v_add_f32_e32 v0, 1.0, v1
	v_mul_f32_e64 v4, |v17|, s1
	v_pack_b32_f16 v110, v22, v2
	v_alignbit_b32 v111, v3, v2, 16
	v_fma_mixhi_f16 v113, v8, s0, v9
	v_log_f32_e32 v47, v0
	ds_read_b128 v[0:3], v108
	v_exp_f32_e32 v117, v4
	ds_read_b128 v[4:7], v108 offset:32
	ds_read_b128 v[8:11], v108 offset:64
	ds_read_b128 v[12:15], v108 offset:96
	ds_read_b128 v[18:21], v160 offset:43008
	ds_read_b128 v[22:25], v160 offset:44032
	s_waitcnt lgkmcnt(5)
	v_pk_add_f32 v[0:1], v[0:1], v[96:97]
	v_pk_add_f32 v[2:3], v[2:3], v[98:99]
	s_waitcnt lgkmcnt(4)
	v_pk_add_f32 v[4:5], v[4:5], v[92:93]
	v_pk_add_f32 v[6:7], v[6:7], v[94:95]
	s_waitcnt lgkmcnt(3)
	v_pk_add_f32 v[8:9], v[8:9], v[88:89]
	v_pk_add_f32 v[10:11], v[10:11], v[90:91]
	s_waitcnt lgkmcnt(2)
	v_pk_add_f32 v[12:13], v[12:13], v[84:85]
	v_pk_add_f32 v[14:15], v[14:15], v[86:87]
	v_max_f32_e32 v16, v16, v16
	v_max_f32_e32 v115, 0, v16
	s_waitcnt lgkmcnt(1)
	v_mfma_f32_32x32x16_f16 v[0:15], v[18:21], v[100:103], v[0:15]
	v_add_f32_e32 v16, 1.0, v117
	v_log_f32_e32 v88, v16
	v_max_f32_e32 v16, v17, v17
	v_max_f32_e32 v89, 0, v16
	ds_read_b128 v[16:19], v160 offset:45056
	v_pk_fma_f32 v[20:21], v[26:27], s[0:1], v[28:29] op_sel_hi:[1,0,1]
	s_waitcnt lgkmcnt(1)
	v_mfma_f32_32x32x16_f16 v[0:15], v[22:25], v[104:107], v[0:15]
	v_fma_mixlo_f16 v22, v109, s0, v116
	v_cvt_pk_f16_f32 v24, v20, v21
	v_fma_f32 v20, v30, s0, v32
	v_fma_f32 v21, v31, s0, v33
	v_pack_b32_f16 v84, v22, v24
	v_cvt_pk_f16_f32 v25, v20, v21
	ds_read_b128 v[20:23], v160 offset:46080
	v_alignbit_b32 v85, v25, v24, 16
	s_waitcnt lgkmcnt(1)
	v_mfma_f32_32x32x16_f16 v[0:15], v[16:19], v[110:113], v[0:15]
	v_fma_f32 v16, v46, s0, v114
	v_fma_f32 v17, v47, s0, v115
	v_cvt_pk_f16_f32 v16, v16, v17
	v_lshrrev_b32_e32 v87, 16, v16
	v_alignbit_b32 v86, v16, v25, 16
	v_fma_mixhi_f16 v87, v88, s0, v89
	ds_read_b128 v[16:19], v108 offset:128
	s_waitcnt lgkmcnt(0)
	v_pk_add_f32 v[16:17], v[16:17], v[80:81]
	v_mfma_f32_32x32x16_f16 v[0:15], v[20:23], v[84:87], v[0:15]
	ds_read_b128 v[20:23], v108 offset:160
	ds_read_b128 v[24:27], v108 offset:192
	ds_read_b128 v[28:31], v108 offset:224
	ds_read_b128 v[88:91], v160 offset:47104
	v_add_f32_e64 v18, v18, v82
	v_add_f32_e64 v19, v19, v83
	s_waitcnt lgkmcnt(3)
	v_pk_add_f32 v[20:21], v[20:21], v[42:43]
	v_pk_add_f32 v[22:23], v[22:23], v[44:45]
	s_waitcnt lgkmcnt(2)
	v_pk_add_f32 v[24:25], v[24:25], v[38:39]
	v_pk_add_f32 v[26:27], v[26:27], v[40:41]
	s_waitcnt lgkmcnt(1)
	v_pk_add_f32 v[28:29], v[28:29], v[34:35]
	v_pk_add_f32 v[30:31], v[30:31], v[36:37]
	ds_read_b128 v[32:35], v160 offset:48128
	v_lshl_add_u32 v82, v207, 2, v208
	s_waitcnt lgkmcnt(1)
	v_mfma_f32_32x32x16_f16 v[16:31], v[88:91], v[100:103], v[16:31]
	s_waitcnt lgkmcnt(0)
	v_mfma_f32_32x32x16_f16 v[16:31], v[32:35], v[104:107], v[16:31]
	ds_read_b128 v[32:35], v160 offset:49152
	ds_read_b128 v[36:39], v160 offset:50176
	s_waitcnt lgkmcnt(1)
	v_mfma_f32_32x32x16_f16 v[16:31], v[32:35], v[110:113], v[16:31]
	v_min_i32_e32 v34, 32, v209
	v_lshlrev_b64 v[32:33], 13, v[172:173]
	v_lshlrev_b32_e32 v35, 2, v210
	v_lshl_add_u64 v[32:33], s[14:15], 0, v[32:33]
	v_cmp_lt_i32_e64 s[2:3], v206, v34
	v_lshlrev_b32_e32 v80, 2, v35
	s_waitcnt lgkmcnt(0)
	v_mfma_f32_32x32x16_f16 v[16:31], v[36:39], v[84:87], v[16:31]
	ds_write_b128 v108, v[0:3]
	ds_write_b128 v108, v[4:7] offset:32
	ds_write_b128 v108, v[8:11] offset:64
	ds_write_b128 v108, v[12:15] offset:96
	s_nop 7
	ds_write_b128 v108, v[16:19] offset:128
	ds_write_b128 v108, v[20:23] offset:160
	ds_write_b128 v108, v[24:27] offset:192
	ds_write_b128 v108, v[28:31] offset:224
	v_cmp_lt_i32_e64 s[2:3], v206, v34
	v_cmp_lt_i32_e64 s[4:5], v204, v34
	v_cmp_lt_i32_e64 s[6:7], v203, v34
	v_cmp_lt_i32_e64 s[8:9], v202, v34
	v_cmp_lt_i32_e64 s[10:11], v201, v34
	v_cmp_lt_i32_e64 s[12:13], v200, v34
	v_cmp_lt_i32_e64 s[14:15], v199, v34
	v_cmp_lt_i32_e64 s[16:17], v198, v34
	s_movk_i32 s22, 0x110
	v_add_u32_e32 v35, v82, v205
	ds_read_b128 v[220:223], v35
	v_mad_u32_u24 v36, v204, s22, v82
	ds_read_b128 v[224:227], v36
	v_mad_u32_u24 v35, v203, s22, v82
	ds_read_b128 v[228:231], v35
	v_mad_u32_u24 v36, v202, s22, v82
	ds_read_b128 v[232:235], v36
	v_mad_u32_u24 v35, v201, s22, v82
	ds_read_b128 v[236:239], v35
	v_mad_u32_u24 v36, v200, s22, v82
	ds_read_b128 v[240:243], v36
	v_mad_u32_u24 v35, v199, s22, v82
	ds_read_b128 v[244:247], v35
	v_mad_u32_u24 v36, v198, s22, v82
	ds_read_b128 v[248:251], v36
	v_mov_b32_e32 v81, 0
	v_lshl_add_u64 v[40:41], v[32:33], 0, v[80:81]
	s_mov_b64 s[22:23], 0x1000
	v_lshl_add_u64 v[252:253], v[40:41], 0, s[22:23]
	s_and_saveexec_b64 s[0:1], s[2:3]
	s_waitcnt lgkmcnt(7)
	global_store_dwordx4 v[40:41], v[220:223], off sc1
	s_or_b64 exec, exec, s[0:1]
	s_and_saveexec_b64 s[0:1], s[4:5]
	s_waitcnt lgkmcnt(6)
	global_store_dwordx4 v[40:41], v[224:227], off offset:1024 sc1
	s_or_b64 exec, exec, s[0:1]
	s_and_saveexec_b64 s[0:1], s[6:7]
	s_waitcnt lgkmcnt(5)
	global_store_dwordx4 v[40:41], v[228:231], off offset:2048 sc1
	s_or_b64 exec, exec, s[0:1]
	s_and_saveexec_b64 s[0:1], s[8:9]
	s_waitcnt lgkmcnt(4)
	global_store_dwordx4 v[40:41], v[232:235], off offset:3072 sc1
	s_or_b64 exec, exec, s[0:1]
	s_and_saveexec_b64 s[0:1], s[10:11]
	s_waitcnt lgkmcnt(3)
	global_store_dwordx4 v[252:253], v[236:239], off sc1
	s_or_b64 exec, exec, s[0:1]
	s_and_saveexec_b64 s[0:1], s[12:13]
	s_waitcnt lgkmcnt(2)
	global_store_dwordx4 v[252:253], v[240:243], off offset:1024 sc1
	s_or_b64 exec, exec, s[0:1]
	s_and_saveexec_b64 s[0:1], s[14:15]
	s_waitcnt lgkmcnt(1)
	global_store_dwordx4 v[252:253], v[244:247], off offset:2048 sc1
	s_or_b64 exec, exec, s[0:1]
	s_and_saveexec_b64 s[0:1], s[16:17]
	s_waitcnt lgkmcnt(0)
	global_store_dwordx4 v[252:253], v[248:251], off offset:3072 sc1
	s_or_b64 exec, exec, s[0:1]

.LBB8_31:
	v_or_b32_e32 v81, 0x8800, v160
	ds_read_b128 v[32:35], v81 offset:16384
	v_cvt_pk_f16_f32 v7, v6, v7
	v_cvt_pk_f16_f32 v6, v4, v5
	v_cvt_pk_f16_f32 v5, v2, v3
	v_cvt_pk_f16_f32 v4, v0, v1
	ds_read_b128 v[0:3], v81 offset:17408
	v_cvt_pk_f16_f32 v87, v14, v15
	v_cvt_pk_f16_f32 v86, v12, v13
	v_cvt_pk_f16_f32 v85, v10, v11
	s_waitcnt lgkmcnt(1)
	v_mfma_f32_32x32x16_f16 v[32:47], v[32:35], v[4:7], 0
	v_cvt_pk_f16_f32 v84, v8, v9
	v_cvt_pk_f16_f32 v23, v22, v23
	v_cvt_pk_f16_f32 v22, v20, v21
	v_cvt_pk_f16_f32 v21, v18, v19
	v_cvt_pk_f16_f32 v20, v16, v17
	v_cvt_pk_f16_f32 v19, v30, v31
	v_cvt_pk_f16_f32 v18, v28, v29
	s_waitcnt lgkmcnt(0)
	v_mfma_f32_32x32x16_f16 v[32:47], v[0:3], v[84:87], v[32:47]
	ds_read_b128 v[0:3], v81 offset:18432
	ds_read_b128 v[8:11], v81 offset:19456
	v_cvt_pk_f16_f32 v17, v26, v27
	v_cvt_pk_f16_f32 v16, v24, v25
	v_lshlrev_b64 v[88:89], 11, v[172:173]
	s_waitcnt lgkmcnt(1)
	v_mfma_f32_32x32x16_f16 v[32:47], v[0:3], v[20:23], v[32:47]
	ds_read_b128 v[0:3], v81 offset:20480
	ds_read_b128 v[24:27], v81 offset:21504
	s_waitcnt lgkmcnt(2)
	v_mfma_f32_32x32x16_f16 v[32:47], v[8:11], v[16:19], v[32:47]
	s_nop 11
	v_mul_f32_e32 v8, v32, v72
	v_mul_f32_e32 v9, v33, v73
	v_mul_f32_e32 v10, v34, v74
	v_mul_f32_e32 v11, v35, v75
	v_mul_f32_e32 v12, v36, v76
	v_mul_f32_e32 v13, v37, v77
	v_mul_f32_e32 v14, v38, v78
	v_mul_f32_e32 v15, v39, v79
	v_cvt_pk_f16_f32 v11, v35, v11
	v_cvt_pk_f16_f32 v10, v34, v10
	v_cvt_pk_f16_f32 v9, v33, v9
	v_cvt_pk_f16_f32 v8, v32, v8
	v_cvt_pk_f16_f32 v31, v39, v15
	v_cvt_pk_f16_f32 v30, v38, v14
	v_cvt_pk_f16_f32 v29, v37, v13
	v_cvt_pk_f16_f32 v28, v36, v12
	ds_write_b128 v108, v[8:11]
	s_waitcnt lgkmcnt(2)
	v_mfma_f32_32x32x16_f16 v[0:15], v[0:3], v[4:7], 0
	ds_write_b128 v108, v[28:31] offset:32
	ds_read_b128 v[30:33], v81 offset:22528
	v_mul_f32_e32 v34, v40, v68
	v_mul_f32_e32 v35, v41, v69
	v_mul_f32_e32 v28, v42, v70
	v_mul_f32_e32 v29, v43, v71
	v_cvt_pk_f16_f32 v29, v43, v29
	s_waitcnt lgkmcnt(3)
	v_mfma_f32_32x32x16_f16 v[0:15], v[24:27], v[84:87], v[0:15]
	v_cvt_pk_f16_f32 v28, v42, v28
	v_cvt_pk_f16_f32 v27, v41, v35
	v_cvt_pk_f16_f32 v26, v40, v34
	ds_write_b128 v108, v[26:29] offset:64
	ds_read_b128 v[24:27], v81 offset:23552
	v_mul_f32_e32 v28, v44, v64
	v_mul_f32_e32 v29, v45, v65
	s_waitcnt lgkmcnt(2)
	v_mfma_f32_32x32x16_f16 v[0:15], v[30:33], v[20:23], v[0:15]
	v_mul_f32_e32 v20, v46, v66
	v_mul_f32_e32 v21, v47, v67
	v_cvt_pk_f16_f32 v23, v47, v21
	v_cvt_pk_f16_f32 v22, v46, v20
	v_cvt_pk_f16_f32 v21, v45, v29
	v_cvt_pk_f16_f32 v20, v44, v28
	ds_write_b128 v108, v[20:23] offset:96
	s_waitcnt lgkmcnt(1)
	v_mfma_f32_32x32x16_f16 v[0:15], v[24:27], v[16:19], v[0:15]
	s_nop 11
	v_mul_f32_e32 v16, v0, v60
	v_mul_f32_e32 v17, v1, v61
	v_mul_f32_e32 v18, v2, v62
	v_mul_f32_e32 v19, v3, v63
	v_cvt_pk_f16_f32 v3, v3, v19
	v_cvt_pk_f16_f32 v2, v2, v18
	v_cvt_pk_f16_f32 v1, v1, v17
	v_cvt_pk_f16_f32 v0, v0, v16
	ds_write_b128 v108, v[0:3] offset:128
	v_mul_f32_e32 v0, v4, v56
	v_mul_f32_e32 v1, v5, v57
	v_mul_f32_e32 v2, v6, v58
	v_mul_f32_e32 v3, v7, v59
	v_cvt_pk_f16_f32 v3, v7, v3
	v_cvt_pk_f16_f32 v2, v6, v2
	v_cvt_pk_f16_f32 v1, v5, v1
	v_cvt_pk_f16_f32 v0, v4, v0
	ds_write_b128 v108, v[0:3] offset:160
	v_mul_f32_e32 v0, v8, v52
	v_mul_f32_e32 v1, v9, v53
	v_mul_f32_e32 v2, v10, v54
	v_mul_f32_e32 v3, v11, v55
	v_cvt_pk_f16_f32 v3, v11, v3
	v_cvt_pk_f16_f32 v2, v10, v2
	v_cvt_pk_f16_f32 v1, v9, v1
	v_cvt_pk_f16_f32 v0, v8, v0
	ds_write_b128 v108, v[0:3] offset:192
	v_mul_f32_e32 v0, v12, v48
	v_mul_f32_e32 v1, v13, v49
	v_mul_f32_e32 v2, v14, v50
	v_mul_f32_e32 v3, v15, v51
	v_cvt_pk_f16_f32 v3, v15, v3
	v_cvt_pk_f16_f32 v2, v14, v2
	v_cvt_pk_f16_f32 v1, v13, v1
	v_cvt_pk_f16_f32 v0, v12, v0
	ds_write_b128 v108, v[0:3] offset:224
	v_lshl_add_u64 v[0:1], v[88:89], 2, s[20:21]
	s_movk_i32 s22, 0x110
	v_add_u32_e32 v2, v82, v205
	ds_read_b128 v[220:223], v2
	v_mad_u32_u24 v3, v204, s22, v82
	ds_read_b128 v[224:227], v3
	v_mad_u32_u24 v2, v203, s22, v82
	ds_read_b128 v[228:231], v2
	v_mad_u32_u24 v3, v202, s22, v82
	ds_read_b128 v[232:235], v3
	v_mad_u32_u24 v2, v201, s22, v82
	ds_read_b128 v[236:239], v2
	v_mad_u32_u24 v3, v200, s22, v82
	ds_read_b128 v[240:243], v3
	v_mad_u32_u24 v2, v199, s22, v82
	ds_read_b128 v[244:247], v2
	v_mad_u32_u24 v3, v198, s22, v82
	ds_read_b128 v[248:251], v3
	v_mov_b32_e32 v81, 0
	v_lshl_add_u64 v[6:7], v[0:1], 0, v[80:81]
	s_mov_b64 s[22:23], 0x1000
	v_lshl_add_u64 v[252:253], v[6:7], 0, s[22:23]
	s_and_saveexec_b64 s[0:1], s[2:3]
	s_waitcnt lgkmcnt(7)
	global_store_dwordx4 v[6:7], v[220:223], off sc1
	s_or_b64 exec, exec, s[0:1]
	s_and_saveexec_b64 s[0:1], s[4:5]
	s_waitcnt lgkmcnt(6)
	global_store_dwordx4 v[6:7], v[224:227], off offset:1024 sc1
	s_or_b64 exec, exec, s[0:1]
	s_and_saveexec_b64 s[0:1], s[6:7]
	s_waitcnt lgkmcnt(5)
	global_store_dwordx4 v[6:7], v[228:231], off offset:2048 sc1
	s_or_b64 exec, exec, s[0:1]
	s_and_saveexec_b64 s[0:1], s[8:9]
	s_waitcnt lgkmcnt(4)
	global_store_dwordx4 v[6:7], v[232:235], off offset:3072 sc1
	s_or_b64 exec, exec, s[0:1]
	s_and_saveexec_b64 s[0:1], s[10:11]
	s_waitcnt lgkmcnt(3)
	global_store_dwordx4 v[252:253], v[236:239], off sc1
	s_or_b64 exec, exec, s[0:1]
	s_and_saveexec_b64 s[0:1], s[12:13]
	s_waitcnt lgkmcnt(2)
	global_store_dwordx4 v[252:253], v[240:243], off offset:1024 sc1
	s_or_b64 exec, exec, s[0:1]
	s_and_saveexec_b64 s[0:1], s[14:15]
	s_waitcnt lgkmcnt(1)
	global_store_dwordx4 v[252:253], v[244:247], off offset:2048 sc1
	s_or_b64 exec, exec, s[0:1]
	s_and_saveexec_b64 s[0:1], s[16:17]
	s_waitcnt lgkmcnt(0)
	global_store_dwordx4 v[252:253], v[248:251], off offset:3072 sc1
	s_or_b64 exec, exec, s[0:1]
	s_endpgm

	.amdhsa_kernel _Z6k_nodeILi1ELi0EEvPfS0_PDv2_DF16_PKiPKfS4_S0_S0_S4_S6_PKDv8_DF16_S6_S9_S6_S9_
		.amdhsa_group_segment_fixed_size 59392
		.amdhsa_private_segment_fixed_size 0
		.amdhsa_kernarg_size 120
		.amdhsa_user_sgpr_count 2
		.amdhsa_user_sgpr_dispatch_ptr 0
		.amdhsa_user_sgpr_queue_ptr 0
		.amdhsa_user_sgpr_kernarg_segment_ptr 1
		.amdhsa_user_sgpr_dispatch_id 0
		.amdhsa_user_sgpr_kernarg_preload_length 0
		.amdhsa_user_sgpr_kernarg_preload_offset 0
		.amdhsa_user_sgpr_private_segment_size 0
		.amdhsa_uses_dynamic_stack 0
		.amdhsa_enable_private_segment 0
		.amdhsa_system_sgpr_workgroup_id_x 1
		.amdhsa_system_sgpr_workgroup_id_y 0
		.amdhsa_system_sgpr_workgroup_id_z 0
		.amdhsa_system_sgpr_workgroup_info 0
		.amdhsa_system_vgpr_workitem_id 0
		.amdhsa_next_free_vgpr 254
		.amdhsa_next_free_sgpr 96
		.amdhsa_accum_offset 256
		.amdhsa_reserve_vcc 1
		.amdhsa_float_round_mode_32 0
		.amdhsa_float_round_mode_16_64 0
		.amdhsa_float_denorm_mode_32 3
		.amdhsa_float_denorm_mode_16_64 3
		.amdhsa_dx10_clamp 1
		.amdhsa_ieee_mode 1
		.amdhsa_fp16_overflow 0
		.amdhsa_tg_split 0
		.amdhsa_exception_fp_ieee_invalid_op 0
		.amdhsa_exception_fp_denorm_src 0
		.amdhsa_exception_fp_ieee_div_zero 0
		.amdhsa_exception_fp_ieee_overflow 0
		.amdhsa_exception_fp_ieee_underflow 0
		.amdhsa_exception_fp_ieee_inexact 0
		.amdhsa_exception_int_div_zero 0
	.end_amdhsa_kernel

amdhsa.kernels:
  - .agpr_count:     0
    .args:
      - .actual_access:  read_only
        .address_space:  global
        .offset:         0
        .size:           8
        .value_kind:     global_buffer
      - .actual_access:  write_only
        .address_space:  global
        .offset:         8
        .size:           8
        .value_kind:     global_buffer
      - .offset:         16
        .size:           288
        .value_kind:     by_value
      - .actual_access:  write_only
        .address_space:  global
        .offset:         304
        .size:           8
        .value_kind:     global_buffer
      - .actual_access:  write_only
        .address_space:  global
        .offset:         312
        .size:           8
        .value_kind:     global_buffer
    .group_segment_fixed_size: 1564
    .kernarg_segment_align: 8
    .kernarg_segment_size: 320
    .language:       OpenCL C
    .language_version:
      - 2
      - 0
    .max_flat_workgroup_size: 256
    .name:           _Z8k_bcountPKiPi8PrepArgsPDF16_S3_
    .private_segment_fixed_size: 0
    .sgpr_count:     26
    .sgpr_spill_count: 0
    .symbol:         _Z8k_bcountPKiPi8PrepArgsPDF16_S3_.kd
    .uniform_work_group_size: 1
    .uses_dynamic_stack: false
    .vgpr_count:     26
    .vgpr_spill_count: 0
    .wavefront_size: 64
  - .agpr_count:     0
    .args:
      - .actual_access:  read_only
        .address_space:  global
        .offset:         0
        .size:           8
        .value_kind:     global_buffer
      - .actual_access:  read_only
        .address_space:  global
        .offset:         8
        .size:           8
        .value_kind:     global_buffer
      - .actual_access:  read_only
        .address_space:  global
        .offset:         16
        .size:           8
        .value_kind:     global_buffer
      - .actual_access:  read_only
        .address_space:  global
        .offset:         24
        .size:           8
        .value_kind:     global_buffer
      - .actual_access:  write_only
        .address_space:  global
        .offset:         32
        .size:           8
        .value_kind:     global_buffer
      - .actual_access:  write_only
        .address_space:  global
        .offset:         40
        .size:           8
        .value_kind:     global_buffer
      - .actual_access:  write_only
        .address_space:  global
        .offset:         48
        .size:           8
        .value_kind:     global_buffer
    .group_segment_fixed_size: 19228
    .kernarg_segment_align: 8
    .kernarg_segment_size: 56
    .language:       OpenCL C
    .language_version:
      - 2
      - 0
    .max_flat_workgroup_size: 512
    .name:           _Z10k_bscatterPKfPKiS2_S2_PiP15HIP_vector_typeIfLj2EEPf
    .private_segment_fixed_size: 0
    .sgpr_count:     26
    .sgpr_spill_count: 0
    .symbol:         _Z10k_bscatterPKfPKiS2_S2_PiP15HIP_vector_typeIfLj2EEPf.kd
    .uniform_work_group_size: 1
    .uses_dynamic_stack: false
    .vgpr_count:     196
    .vgpr_spill_count: 0
    .wavefront_size: 64
  - .agpr_count:     0
    .args:
      - .actual_access:  read_only
        .address_space:  global
        .offset:         0
        .size:           8
        .value_kind:     global_buffer
      - .actual_access:  read_only
        .address_space:  global
        .offset:         8
        .size:           8
        .value_kind:     global_buffer
      - .actual_access:  read_only
        .address_space:  global
        .offset:         16
        .size:           8
        .value_kind:     global_buffer
      - .actual_access:  write_only
        .address_space:  global
        .offset:         24
        .size:           8
        .value_kind:     global_buffer
      - .actual_access:  write_only
        .address_space:  global
        .offset:         32
        .size:           8
        .value_kind:     global_buffer
    .group_segment_fixed_size: 1024
    .kernarg_segment_align: 8
    .kernarg_segment_size: 40
    .language:       OpenCL C
    .language_version:
      - 2
      - 0
    .max_flat_workgroup_size: 512
    .name:           _Z7k_bsortPK15HIP_vector_typeIfLj2EEPKiS4_PS_IfLj4EEPi
    .private_segment_fixed_size: 0
    .sgpr_count:     58
    .sgpr_spill_count: 0
    .symbol:         _Z7k_bsortPK15HIP_vector_typeIfLj2EEPKiS4_PS_IfLj4EEPi.kd
    .uniform_work_group_size: 1
    .uses_dynamic_stack: false
    .vgpr_count:     71
    .vgpr_spill_count: 0
    .wavefront_size: 64
  - .agpr_count:     0
    .args:
      - .actual_access:  read_only
        .address_space:  global
        .offset:         0
        .size:           8
        .value_kind:     global_buffer
      - .actual_access:  read_only
        .address_space:  global
        .offset:         8
        .size:           8
        .value_kind:     global_buffer
      - .actual_access:  read_only
        .address_space:  global
        .offset:         16
        .size:           8
        .value_kind:     global_buffer
      - .actual_access:  read_only
        .address_space:  global
        .offset:         24
        .size:           8
        .value_kind:     global_buffer
      - .actual_access:  read_only
        .address_space:  global
        .offset:         32
        .size:           8
        .value_kind:     global_buffer
      - .actual_access:  read_only
        .address_space:  global
        .offset:         40
        .size:           8
        .value_kind:     global_buffer
      - .actual_access:  write_only
        .address_space:  global
        .offset:         48
        .size:           8
        .value_kind:     global_buffer
      - .actual_access:  write_only
        .address_space:  global
        .offset:         56
        .size:           8
        .value_kind:     global_buffer
      - .offset:         64
        .size:           4
        .value_kind:     hidden_block_count_x
      - .offset:         68
        .size:           4
        .value_kind:     hidden_block_count_y
      - .offset:         72
        .size:           4
        .value_kind:     hidden_block_count_z
      - .offset:         76
        .size:           2
        .value_kind:     hidden_group_size_x
      - .offset:         78
        .size:           2
        .value_kind:     hidden_group_size_y
      - .offset:         80
        .size:           2
        .value_kind:     hidden_group_size_z
      - .offset:         82
        .size:           2
        .value_kind:     hidden_remainder_x
      - .offset:         84
        .size:           2
        .value_kind:     hidden_remainder_y
      - .offset:         86
        .size:           2
        .value_kind:     hidden_remainder_z
      - .offset:         104
        .size:           8
        .value_kind:     hidden_global_offset_x
      - .offset:         112
        .size:           8
        .value_kind:     hidden_global_offset_y
      - .offset:         120
        .size:           8
        .value_kind:     hidden_global_offset_z
      - .offset:         128
        .size:           2
        .value_kind:     hidden_grid_dims
    .group_segment_fixed_size: 31488
    .kernarg_segment_align: 8
    .kernarg_segment_size: 320
    .language:       OpenCL C
    .language_version:
      - 2
      - 0
    .max_flat_workgroup_size: 256
    .name:           _Z7k_edge0PK15HIP_vector_typeIfLj4EEPKDv8_DF16_S5_PKfS7_S7_PfS8_
    .private_segment_fixed_size: 0
    .sgpr_count:     59
    .sgpr_spill_count: 0
    .symbol:         _Z7k_edge0PK15HIP_vector_typeIfLj4EEPKDv8_DF16_S5_PKfS7_S7_PfS8_.kd
    .uniform_work_group_size: 1
    .uses_dynamic_stack: false
    .vgpr_count:     96
    .vgpr_spill_count: 0
    .wavefront_size: 64
  - .agpr_count:     0
    .args:
      - .actual_access:  read_only
        .address_space:  global
        .offset:         0
        .size:           8
        .value_kind:     global_buffer
      - .actual_access:  read_only
        .address_space:  global
        .offset:         8
        .size:           8
        .value_kind:     global_buffer
      - .actual_access:  read_only
        .address_space:  global
        .offset:         16
        .size:           8
        .value_kind:     global_buffer
      - .actual_access:  read_only
        .address_space:  global
        .offset:         24
        .size:           8
        .value_kind:     global_buffer
      - .actual_access:  read_only
        .address_space:  global
        .offset:         32
        .size:           8
        .value_kind:     global_buffer
      - .actual_access:  read_only
        .address_space:  global
        .offset:         40
        .size:           8
        .value_kind:     global_buffer
      - .address_space:  global
        .offset:         48
        .size:           8
        .value_kind:     global_buffer
      - .actual_access:  write_only
        .address_space:  global
        .offset:         56
        .size:           8
        .value_kind:     global_buffer
      - .actual_access:  write_only
        .address_space:  global
        .offset:         64
        .size:           8
        .value_kind:     global_buffer
      - .offset:         72
        .size:           4
        .value_kind:     hidden_block_count_x
      - .offset:         76
        .size:           4
        .value_kind:     hidden_block_count_y
      - .offset:         80
        .size:           4
        .value_kind:     hidden_block_count_z
      - .offset:         84
        .size:           2
        .value_kind:     hidden_group_size_x
      - .offset:         86
        .size:           2
        .value_kind:     hidden_group_size_y
      - .offset:         88
        .size:           2
        .value_kind:     hidden_group_size_z
      - .offset:         90
        .size:           2
        .value_kind:     hidden_remainder_x
      - .offset:         92
        .size:           2
        .value_kind:     hidden_remainder_y
      - .offset:         94
        .size:           2
        .value_kind:     hidden_remainder_z
      - .offset:         112
        .size:           8
        .value_kind:     hidden_global_offset_x
      - .offset:         120
        .size:           8
        .value_kind:     hidden_global_offset_y
      - .offset:         128
        .size:           8
        .value_kind:     hidden_global_offset_z
      - .offset:         136
        .size:           2
        .value_kind:     hidden_grid_dims
    .group_segment_fixed_size: 31488
    .kernarg_segment_align: 8
    .kernarg_segment_size: 328
    .language:       OpenCL C
    .language_version:
      - 2
      - 0
    .max_flat_workgroup_size: 256
    .name:           _Z7k_edge1PK15HIP_vector_typeIfLj4EEPKDv8_DF16_S5_PKfS7_S7_PKDv2_DF16_PfSB_
    .private_segment_fixed_size: 0
    .sgpr_count:     56
    .sgpr_spill_count: 0
    .symbol:         _Z7k_edge1PK15HIP_vector_typeIfLj4EEPKDv8_DF16_S5_PKfS7_S7_PKDv2_DF16_PfSB_.kd
    .uniform_work_group_size: 1
    .uses_dynamic_stack: false
    .vgpr_count:     128
    .vgpr_spill_count: 0
    .wavefront_size: 64
  - .agpr_count:     0
    .args:
      - .actual_access:  read_only
        .address_space:  global
        .offset:         0
        .size:           8
        .value_kind:     global_buffer
      - .actual_access:  read_only
        .address_space:  global
        .offset:         8
        .size:           8
        .value_kind:     global_buffer
      - .address_space:  global
        .offset:         16
        .size:           8
        .value_kind:     global_buffer
      - .address_space:  global
        .offset:         24
        .size:           8
        .value_kind:     global_buffer
    .group_segment_fixed_size: 0
    .kernarg_segment_align: 8
    .kernarg_segment_size: 32
    .language:       OpenCL C
    .language_version:
      - 2
      - 0
    .max_flat_workgroup_size: 256
    .name:           _Z6k_poolPKfPKiPfS3_
    .private_segment_fixed_size: 0
    .sgpr_count:     20
    .sgpr_spill_count: 0
    .symbol:         _Z6k_poolPKfPKiPfS3_.kd
    .uniform_work_group_size: 1
    .uses_dynamic_stack: false
    .vgpr_count:     16
    .vgpr_spill_count: 0
    .wavefront_size: 64
  - .agpr_count:     0
    .args:
      - .actual_access:  read_only
        .address_space:  global
        .offset:         0
        .size:           8
        .value_kind:     global_buffer
      - .actual_access:  read_only
        .address_space:  global
        .offset:         8
        .size:           8
        .value_kind:     global_buffer
      - .actual_access:  read_only
        .address_space:  global
        .offset:         16
        .size:           8
        .value_kind:     global_buffer
      - .actual_access:  read_only
        .address_space:  global
        .offset:         24
        .size:           8
        .value_kind:     global_buffer
      - .actual_access:  read_only
        .address_space:  global
        .offset:         32
        .size:           8
        .value_kind:     global_buffer
      - .actual_access:  read_only
        .address_space:  global
        .offset:         40
        .size:           8
        .value_kind:     global_buffer
      - .actual_access:  write_only
        .address_space:  global
        .offset:         48
        .size:           8
        .value_kind:     global_buffer
    .group_segment_fixed_size: 20480
    .kernarg_segment_align: 8
    .kernarg_segment_size: 56
    .language:       OpenCL C
    .language_version:
      - 2
      - 0
    .max_flat_workgroup_size: 64
    .name:           _Z7k_finalPKfS0_S0_S0_S0_S0_Pf
    .private_segment_fixed_size: 0
    .sgpr_count:     42
    .sgpr_spill_count: 0
    .symbol:         _Z7k_finalPKfS0_S0_S0_S0_S0_Pf.kd
    .uniform_work_group_size: 1
    .uses_dynamic_stack: false
    .vgpr_count:     144
    .vgpr_spill_count: 0
    .wavefront_size: 64
  - .agpr_count:     0
    .args:
      - .actual_access:  read_only
        .address_space:  global
        .offset:         0
        .size:           8
        .value_kind:     global_buffer
      - .address_space:  global
        .offset:         8
        .size:           8
        .value_kind:     global_buffer
      - .address_space:  global
        .offset:         16
        .size:           8
        .value_kind:     global_buffer
      - .actual_access:  read_only
        .address_space:  global
        .offset:         24
        .size:           8
        .value_kind:     global_buffer
      - .actual_access:  read_only
        .address_space:  global
        .offset:         32
        .size:           8
        .value_kind:     global_buffer
      - .actual_access:  read_only
        .address_space:  global
        .offset:         40
        .size:           8
        .value_kind:     global_buffer
      - .actual_access:  read_only
        .address_space:  global
        .offset:         48
        .size:           8
        .value_kind:     global_buffer
      - .actual_access:  read_only
        .address_space:  global
        .offset:         56
        .size:           8
        .value_kind:     global_buffer
      - .actual_access:  read_only
        .address_space:  global
        .offset:         64
        .size:           8
        .value_kind:     global_buffer
      - .actual_access:  read_only
        .address_space:  global
        .offset:         72
        .size:           8
        .value_kind:     global_buffer
      - .actual_access:  read_only
        .address_space:  global
        .offset:         80
        .size:           8
        .value_kind:     global_buffer
      - .actual_access:  read_only
        .address_space:  global
        .offset:         88
        .size:           8
        .value_kind:     global_buffer
      - .actual_access:  read_only
        .address_space:  global
        .offset:         96
        .size:           8
        .value_kind:     global_buffer
      - .actual_access:  read_only
        .address_space:  global
        .offset:         104
        .size:           8
        .value_kind:     global_buffer
      - .actual_access:  read_only
        .address_space:  global
        .offset:         112
        .size:           8
        .value_kind:     global_buffer
    .group_segment_fixed_size: 59392
    .kernarg_segment_align: 8
    .kernarg_segment_size: 120
    .language:       OpenCL C
    .language_version:
      - 2
      - 0
    .max_flat_workgroup_size: 256
    .name:           _Z6k_nodeILi0ELi0EEvPfS0_PDv2_DF16_PKiPKfS4_S0_S0_S4_S6_PKDv8_DF16_S6_S9_S6_S9_
    .private_segment_fixed_size: 0
    .sgpr_count:     30
    .sgpr_spill_count: 0
    .symbol:         _Z6k_nodeILi0ELi0EEvPfS0_PDv2_DF16_PKiPKfS4_S0_S0_S4_S6_PKDv8_DF16_S6_S9_S6_S9_.kd
    .uniform_work_group_size: 1
    .uses_dynamic_stack: false
    .vgpr_count:     190
    .vgpr_spill_count: 0
    .wavefront_size: 64
  - .agpr_count:     0
    .args:
      - .actual_access:  read_only
        .address_space:  global
        .offset:         0
        .size:           8
        .value_kind:     global_buffer
      - .address_space:  global
        .offset:         8
        .size:           8
        .value_kind:     global_buffer
      - .address_space:  global
        .offset:         16
        .size:           8
        .value_kind:     global_buffer
      - .actual_access:  read_only
        .address_space:  global
        .offset:         24
        .size:           8
        .value_kind:     global_buffer
      - .actual_access:  read_only
        .address_space:  global
        .offset:         32
        .size:           8
        .value_kind:     global_buffer
      - .actual_access:  read_only
        .address_space:  global
        .offset:         40
        .size:           8
        .value_kind:     global_buffer
      - .actual_access:  read_only
        .address_space:  global
        .offset:         48
        .size:           8
        .value_kind:     global_buffer
      - .actual_access:  read_only
        .address_space:  global
        .offset:         56
        .size:           8
        .value_kind:     global_buffer
      - .actual_access:  read_only
        .address_space:  global
        .offset:         64
        .size:           8
        .value_kind:     global_buffer
      - .actual_access:  read_only
        .address_space:  global
        .offset:         72
        .size:           8
        .value_kind:     global_buffer
      - .actual_access:  read_only
        .address_space:  global
        .offset:         80
        .size:           8
        .value_kind:     global_buffer
      - .actual_access:  read_only
        .address_space:  global
        .offset:         88
        .size:           8
        .value_kind:     global_buffer
      - .actual_access:  read_only
        .address_space:  global
        .offset:         96
        .size:           8
        .value_kind:     global_buffer
      - .actual_access:  read_only
        .address_space:  global
        .offset:         104
        .size:           8
        .value_kind:     global_buffer
      - .actual_access:  read_only
        .address_space:  global
        .offset:         112
        .size:           8
        .value_kind:     global_buffer
    .group_segment_fixed_size: 59392
    .kernarg_segment_align: 8
    .kernarg_segment_size: 120
    .language:       OpenCL C
    .language_version:
      - 2
      - 0
    .max_flat_workgroup_size: 256
    .name:           _Z6k_nodeILi1ELi0EEvPfS0_PDv2_DF16_PKiPKfS4_S0_S0_S4_S6_PKDv8_DF16_S6_S9_S6_S9_
    .private_segment_fixed_size: 0
    .sgpr_count:     30
    .sgpr_spill_count: 0
    .symbol:         _Z6k_nodeILi1ELi0EEvPfS0_PDv2_DF16_PKiPKfS4_S0_S0_S4_S6_PKDv8_DF16_S6_S9_S6_S9_.kd
    .uniform_work_group_size: 1
    .uses_dynamic_stack: false
    .vgpr_count:     254
    .vgpr_spill_count: 0
    .wavefront_size: 64
  - .agpr_count:     0
    .args:
      - .actual_access:  read_only
        .address_space:  global
        .offset:         0
        .size:           8
        .value_kind:     global_buffer
      - .actual_access:  read_only
        .address_space:  global
        .offset:         8
        .size:           8
        .value_kind:     global_buffer
      - .address_space:  global
        .offset:         16
        .size:           8
        .value_kind:     global_buffer
      - .actual_access:  read_only
        .address_space:  global
        .offset:         24
        .size:           8
        .value_kind:     global_buffer
      - .actual_access:  read_only
        .address_space:  global
        .offset:         32
        .size:           8
        .value_kind:     global_buffer
      - .actual_access:  read_only
        .address_space:  global
        .offset:         40
        .size:           8
        .value_kind:     global_buffer
      - .address_space:  global
        .offset:         48
        .size:           8
        .value_kind:     global_buffer
      - .address_space:  global
        .offset:         56
        .size:           8
        .value_kind:     global_buffer
      - .actual_access:  read_only
        .address_space:  global
        .offset:         64
        .size:           8
        .value_kind:     global_buffer
      - .actual_access:  read_only
        .address_space:  global
        .offset:         72
        .size:           8
        .value_kind:     global_buffer
      - .actual_access:  read_only
        .address_space:  global
        .offset:         80
        .size:           8
        .value_kind:     global_buffer
      - .actual_access:  read_only
        .address_space:  global
        .offset:         88
        .size:           8
        .value_kind:     global_buffer
      - .actual_access:  read_only
        .address_space:  global
        .offset:         96
        .size:           8
        .value_kind:     global_buffer
      - .actual_access:  read_only
        .address_space:  global
        .offset:         104
        .size:           8
        .value_kind:     global_buffer
      - .actual_access:  read_only
        .address_space:  global
        .offset:         112
        .size:           8
        .value_kind:     global_buffer
    .group_segment_fixed_size: 59392
    .kernarg_segment_align: 8
    .kernarg_segment_size: 120
    .language:       OpenCL C
    .language_version:
      - 2
      - 0
    .max_flat_workgroup_size: 256
    .name:           _Z6k_nodeILi1ELi1EEvPfS0_PDv2_DF16_PKiPKfS4_S0_S0_S4_S6_PKDv8_DF16_S6_S9_S6_S9_
    .private_segment_fixed_size: 0
    .sgpr_count:     30
    .sgpr_spill_count: 0
    .symbol:         _Z6k_nodeILi1ELi1EEvPfS0_PDv2_DF16_PKiPKfS4_S0_S0_S4_S6_PKDv8_DF16_S6_S9_S6_S9_.kd
    .uniform_work_group_size: 1
    .uses_dynamic_stack: false
    .vgpr_count:     220
    .vgpr_spill_count: 0
    .wavefront_size: 64
